# speedup vs baseline: 1.0783x; 1.0034x over previous
.LBB3_2:
	s_or_b64 exec, exec, s[8:9]
	v_and_b32_e32 v6, 31, v0
	v_add_u32_e32 v2, v124, v6
	s_bfe_u32 s33, s2, 0x30003
	v_min_u32_e32 v2, 0x2045f, v2
	v_and_b32_e32 v10, 7, v0
	s_mul_i32 s14, s33, 0xc0
	v_lshrrev_b32_e32 v42, 3, v0
	v_lshlrev_b32_e32 v2, 3, v2
	v_lshlrev_b32_e32 v108, 4, v10
	v_or_b32_e32 v5, s14, v42
	global_load_dwordx2 v[28:29], v2, s[68:69]
	v_lshl_add_u64 v[2:3], s[6:7], 0, v[108:109]
	v_lshlrev_b32_e32 v108, 7, v5
	v_or_b32_e32 v5, 0x100, v0
	v_lshrrev_b32_e32 v43, 3, v5
	v_or_b32_e32 v5, s14, v43
	v_lshl_add_u64 v[8:9], v[2:3], 0, v[108:109]
	v_lshlrev_b32_e32 v108, 7, v5
	v_or_b32_e32 v5, 0x200, v0
	v_lshrrev_b32_e32 v44, 3, v5
	v_or_b32_e32 v5, 0x300, v0
	v_lshl_add_u64 v[14:15], v[2:3], 0, v[108:109]
	v_add_lshl_u32 v108, v44, s14, 7
	v_lshrrev_b32_e32 v45, 3, v5
	global_load_dwordx4 v[16:19], v[8:9], off
	global_load_dwordx4 v[20:23], v[14:15], off
	v_lshl_add_u64 v[8:9], v[2:3], 0, v[108:109]
	v_add_lshl_u32 v108, v45, s14, 7
	v_lshl_add_u64 v[14:15], v[2:3], 0, v[108:109]
	global_load_dwordx4 v[24:27], v[8:9], off
	global_load_dwordx4 v[30:33], v[14:15], off
	v_or_b32_e32 v15, 0x80, v42
	v_or_b32_e32 v5, 0x500, v0
	v_add_lshl_u32 v108, v15, s14, 7
	v_lshrrev_b32_e32 v46, 3, v5
	v_lshl_add_u64 v[8:9], v[2:3], 0, v[108:109]
	v_add_lshl_u32 v108, v46, s14, 7
	v_lshl_add_u64 v[2:3], v[2:3], 0, v[108:109]
	global_load_dwordx4 v[34:37], v[8:9], off
	global_load_dwordx4 v[38:41], v[2:3], off
	v_lshrrev_b32_e32 v11, 5, v4
	v_min_u32_e32 v2, 16, v6
	v_lshlrev_b32_e32 v9, 2, v11
	v_mul_u32_u24_e32 v5, 17, v2
	v_add_lshl_u32 v108, v9, v5, 2
	s_waitcnt lgkmcnt(0)
	global_load_dword v14, v108, s[4:5]
	v_lshrrev_b16_e32 v8, 1, v42
	v_mad_u64_u32 v[2:3], s[6:7], s33, 17, v[6:7]
	v_and_b32_e32 v3, 3, v8
	v_mul_u32_u24_e32 v8, 17, v2
	v_bfrev_b32_e32 v2, v3
	v_bfe_u32 v47, v0, 6, 1
	v_lshrrev_b32_e32 v2, 29, v2
	v_bitop3_b32 v2, v47, v10, v2 bitop3:0x36
	v_lshlrev_b32_e32 v2, 4, v2
	v_cmp_gt_u32_e64 s[64:65], 17, v6
	v_lshl_or_b32 v42, v42, 7, v2
	v_lshl_or_b32 v43, v43, 7, v2
	v_lshl_or_b32 v44, v44, 7, v2
	v_lshl_or_b32 v45, v45, 7, v2
	v_lshl_or_b32 v15, v15, 7, v2
	v_lshl_or_b32 v46, v46, 7, v2
	v_lshl_add_u64 v[2:3], s[4:5], 0, v[108:109]
	v_add_lshl_u32 v9, v9, v8, 2
	s_waitcnt vmcnt(6)
	ds_write_b128 v42, v[16:19]
	s_waitcnt vmcnt(5)
	ds_write_b128 v43, v[20:23]
	s_waitcnt vmcnt(4)
	ds_write_b128 v44, v[24:27]
	s_waitcnt vmcnt(3)
	ds_write_b128 v45, v[30:33]
	s_waitcnt vmcnt(2)
	ds_write_b128 v15, v[34:37]
	s_waitcnt vmcnt(1)
	ds_write_b128 v46, v[38:41]
	v_mov_b32_e32 v108, 0
	v_mov_b32_e32 v117, 0
	v_mov_b32_e32 v118, 0
	v_mov_b32_e32 v119, 0
	v_mov_b32_e32 v120, 0
	v_mov_b32_e32 v121, 0
	v_mov_b32_e32 v122, 0
	global_load_dword v15, v[2:3], off offset:4
	global_load_dword v16, v[2:3], off offset:8
	global_load_dword v17, v[2:3], off offset:12
	global_load_dword v18, v[2:3], off offset:32
	global_load_dword v19, v[2:3], off offset:36
	global_load_dword v21, v[2:3], off offset:40
	global_load_dword v23, v[2:3], off offset:44
	s_and_saveexec_b64 s[8:9], s[64:65]
	global_load_dword v48, v9, s[70:71]
	global_load_dword v49, v9, s[70:71] offset:4
	global_load_dword v50, v9, s[70:71] offset:8
	global_load_dword v51, v9, s[70:71] offset:12
	global_load_dword v52, v9, s[70:71] offset:32
	global_load_dword v53, v9, s[70:71] offset:36
	global_load_dword v54, v9, s[70:71] offset:40
	global_load_dword v55, v9, s[70:71] offset:44
	s_or_b64 exec, exec, s[8:9]
	v_lshlrev_b32_e32 v2, 2, v5
	global_load_dword v24, v2, s[4:5] offset:64
	v_mov_b32_e32 v2, 0xf149f2ca
	v_cmp_gt_u32_e64 s[62:63], 32, v4
	v_cndmask_b32_e64 v123, 0, v2, s[64:65]
	v_cmp_lt_u32_e64 s[6:7], 31, v4
	s_and_b64 s[4:5], s[64:65], s[62:63]
	s_and_saveexec_b64 s[8:9], s[4:5]
	v_lshlrev_b32_e32 v2, 2, v8
	global_load_dword v56, v2, s[70:71] offset:64
	s_or_b64 exec, exec, s[8:9]
	s_waitcnt vmcnt(0)
	s_and_saveexec_b64 s[8:9], s[64:65]
	v_mul_f32_e32 v109, 0x3fb8aa3b, v48
	v_mul_f32_e32 v117, 0x3fb8aa3b, v49
	v_mul_f32_e32 v108, 0x3fb8aa3b, v50
	v_mul_f32_e32 v119, 0x3fb8aa3b, v51
	v_mul_f32_e32 v118, 0x3fb8aa3b, v52
	v_mul_f32_e32 v121, 0x3fb8aa3b, v53
	v_mul_f32_e32 v120, 0x3fb8aa3b, v54
	v_mul_f32_e32 v122, 0x3fb8aa3b, v55
	s_or_b64 exec, exec, s[8:9]
	s_and_saveexec_b64 s[8:9], s[4:5]
	v_mul_f32_e32 v123, 0x3fb8aa3b, v56
	s_or_b64 exec, exec, s[8:9]
	v_cmp_ne_u32_e32 vcc, 1, v1
	v_lshlrev_b32_e32 v20, 4, v4
	s_and_saveexec_b64 s[8:9], vcc
	s_xor_b64 s[8:9], exec, s[8:9]
	v_lshlrev_b32_e32 v20, 4, v4
	s_or_saveexec_b64 s[8:9], s[8:9]
	s_load_dwordx2 s[66:67], s[0:1], 0x38
	v_lshlrev_b32_e32 v22, 3, v10
	s_xor_b64 exec, exec, s[8:9]
	s_cbranch_execz .LBB3_36
	s_load_dwordx2 s[10:11], s[0:1], 0x10
	s_and_saveexec_b64 s[12:13], s[6:7]
	s_xor_b64 s[12:13], exec, s[12:13]
	v_mov_b32_e32 v2, 0
	v_mov_b32_e32 v3, v2
	v_mov_b32_e32 v4, v2
	v_mov_b32_e32 v5, v2
	ds_write_b128 v20, v[2:5] offset:43008
	s_or_saveexec_b64 s[12:13], s[12:13]
	v_or_b32_e32 v3, s14, v6
	v_mov_b32_e32 v2, 0
	v_lshlrev_b32_e32 v8, 2, v3
	v_mov_b32_e32 v3, 0
	v_mov_b32_e32 v4, 0
	v_mov_b32_e32 v5, 0
	s_xor_b64 exec, exec, s[12:13]
	s_cbranch_execz .LBB3_27
	v_mov_b32_e32 v9, 0
	s_waitcnt lgkmcnt(0)
	v_lshl_add_u64 v[2:3], s[10:11], 0, v[8:9]
	v_add_co_u32_e32 v4, vcc, 0x1000, v2
	v_mov_b32_e32 v32, v9
	s_nop 0
	v_addc_co_u32_e32 v5, vcc, 0, v3, vcc
	v_add_co_u32_e32 v2, vcc, 0x3000, v2
	v_mov_b32_e32 v33, v9
	s_nop 0
	v_addc_co_u32_e32 v3, vcc, 0, v3, vcc
	global_load_dword v25, v8, s[10:11]
	global_load_dword v26, v[2:3], off
	global_load_dword v27, v8, s[10:11] offset:128
	global_load_dword v30, v[2:3], off offset:128
	global_load_dword v31, v[4:5], off offset:2048
	global_load_dword v34, v[4:5], off offset:2176
	v_mov_b32_e32 v4, v9
	s_waitcnt vmcnt(4)
	v_cvt_f16_f32_e32 v3, v26
	s_waitcnt vmcnt(2)
	v_cvt_f16_f32_e32 v5, v30
	s_waitcnt vmcnt(1)
	v_cvt_pk_f16_f32 v30, v25, -v31
	s_waitcnt vmcnt(0)
	v_cvt_pk_f16_f32 v2, v27, -v34
	v_pack_b32_f16 v31, v3, 0
	v_pack_b32_f16 v3, v5, 0
	v_mov_b32_e32 v5, v9
	ds_write_b128 v20, v[30:33] offset:43008
